# speedup vs baseline: 1.0832x; 1.0513x over previous
.LBB1_3:
	s_waitcnt lgkmcnt(0)
	s_barrier
	s_add_i32 s20, s20, 1
	s_add_i32 s18, s18, 2
	s_cmp_eq_u32 s20, 30
	s_cbranch_scc1 .Lt30
.LBB1_4:
	v_add_u32_e32 v182, s19, v191
	v_add_u32_e32 v238, s19, v192
	ds_read_b128 v[178:181], v182 offset:32768
	ds_read_b128 v[194:197], v182 offset:34816
	ds_read_b128 v[198:201], v182 offset:36864
	ds_read_b128 v[202:205], v182 offset:38912
	ds_read_b128 v[206:209], v238
	ds_read_b128 v[210:213], v238 offset:2048
	ds_read_b128 v[214:217], v238 offset:4096
	ds_read_b128 v[218:221], v238 offset:6144
	ds_read_b128 v[222:225], v238 offset:8192
	ds_read_b128 v[226:229], v238 offset:10240
	ds_read_b128 v[230:233], v238 offset:12288
	ds_read_b128 v[234:237], v238 offset:14336
	s_min_u32 s21, s20, 29
	s_xor_b32 s19, s19, 0x10000
	v_add_u32_e32 v239, s19, v189
	s_waitcnt vmcnt(11)
	v_cvt_pk_bf16_f32 v13, v12, v13
	v_cvt_pk_bf16_f32 v12, v10, v11
	s_waitcnt vmcnt(10)
	v_cvt_pk_bf16_f32 v11, v20, v21
	v_cvt_pk_bf16_f32 v10, v18, v19
	ds_write2st64_b64 v239, v[12:13], v[10:11] offset1:8
	s_waitcnt vmcnt(9)
	v_cvt_pk_bf16_f32 v11, v24, v25
	v_cvt_pk_bf16_f32 v10, v22, v23
	s_waitcnt vmcnt(8)
	v_cvt_pk_bf16_f32 v13, v32, v33
	v_cvt_pk_bf16_f32 v12, v30, v31
	ds_write2st64_b64 v239, v[10:11], v[12:13] offset0:16 offset1:24
	s_waitcnt vmcnt(7)
	v_cvt_pk_bf16_f32 v11, v36, v37
	v_cvt_pk_bf16_f32 v10, v34, v35
	s_waitcnt vmcnt(6)
	v_cvt_pk_bf16_f32 v13, v40, v41
	v_cvt_pk_bf16_f32 v12, v38, v39
	ds_write2st64_b64 v239, v[10:11], v[12:13] offset0:32 offset1:40
	s_waitcnt vmcnt(5)
	v_cvt_pk_bf16_f32 v11, v44, v45
	v_cvt_pk_bf16_f32 v10, v42, v43
	s_waitcnt vmcnt(4)
	v_cvt_pk_bf16_f32 v13, v48, v49
	v_cvt_pk_bf16_f32 v12, v46, v47
	ds_write2st64_b64 v239, v[10:11], v[12:13] offset0:48 offset1:56
	s_waitcnt lgkmcnt(0)
	s_add_i32 s21, s21, 2
	s_barrier
	s_setprio 1
	s_lshl_b32 s22, s21, 1
	s_and_b32 s22, s22, 0x60
	s_add_i32 s22, s22, s12
	s_lshl_b32 s22, s22, 6
	s_and_b32 s22, s22, 0x3f00
	s_or_b32 s22, s22, s13
	s_lshl_b32 s23, s21, 23
	s_lshl_b32 s22, s22, 9
	s_and_b32 s23, s23, 0x7000000
	s_or_b32 s22, s22, s23
	s_lshl_b32 s23, s21, 8
	s_and_b32 s23, s23, 0x100
	s_or_b32 s22, s22, s23
	s_or_b32 s23, s22, 0x4000
	s_waitcnt lgkmcnt(11)
	v_mfma_f32_16x16x32_bf16 v[174:177], v[178:181], v[206:209], v[174:177]
	v_mfma_f32_16x16x32_bf16 v[170:173], v[194:197], v[206:209], v[170:173]
	v_mfma_f32_16x16x32_bf16 v[158:161], v[198:201], v[206:209], v[158:161]
	buffer_load_dwordx4 v[10:13], v1, s[4:7], s22 offen sc0 nt
	v_mfma_f32_16x16x32_bf16 v[142:145], v[202:205], v[206:209], v[142:145]
	s_waitcnt lgkmcnt(10)
	v_mfma_f32_16x16x32_bf16 v[166:169], v[178:181], v[210:213], v[166:169]
	v_mfma_f32_16x16x32_bf16 v[162:165], v[194:197], v[210:213], v[162:165]
	v_mfma_f32_16x16x32_bf16 v[146:149], v[198:201], v[210:213], v[146:149]
	buffer_load_dwordx4 v[18:21], v1, s[4:7], s23 offen sc0 nt
	s_or_b32 s23, s22, 0x8000
	v_mfma_f32_16x16x32_bf16 v[122:125], v[202:205], v[210:213], v[122:125]
	s_waitcnt lgkmcnt(9)
	v_mfma_f32_16x16x32_bf16 v[154:157], v[178:181], v[214:217], v[154:157]
	v_mfma_f32_16x16x32_bf16 v[150:153], v[194:197], v[214:217], v[150:153]
	v_mfma_f32_16x16x32_bf16 v[130:133], v[198:201], v[214:217], v[130:133]
	buffer_load_dwordx4 v[22:25], v1, s[4:7], s23 offen sc0 nt
	s_or_b32 s23, s22, 0xc000
	v_mfma_f32_16x16x32_bf16 v[106:109], v[202:205], v[214:217], v[106:109]
	s_waitcnt lgkmcnt(8)
	v_mfma_f32_16x16x32_bf16 v[138:141], v[178:181], v[218:221], v[138:141]
	v_mfma_f32_16x16x32_bf16 v[134:137], v[194:197], v[218:221], v[134:137]
	v_mfma_f32_16x16x32_bf16 v[114:117], v[198:201], v[218:221], v[114:117]
	buffer_load_dwordx4 v[30:33], v1, s[4:7], s23 offen sc0 nt
	s_or_b32 s23, s22, 0x10000
	v_mfma_f32_16x16x32_bf16 v[90:93], v[202:205], v[218:221], v[90:93]
	s_waitcnt lgkmcnt(7)
	v_mfma_f32_16x16x32_bf16 v[126:129], v[178:181], v[222:225], v[126:129]
	v_mfma_f32_16x16x32_bf16 v[118:121], v[194:197], v[222:225], v[118:121]
	v_mfma_f32_16x16x32_bf16 v[98:101], v[198:201], v[222:225], v[98:101]
	buffer_load_dwordx4 v[34:37], v1, s[4:7], s23 offen sc0 nt
	s_or_b32 s23, s22, 0x14000
	v_mfma_f32_16x16x32_bf16 v[74:77], v[202:205], v[222:225], v[74:77]
	s_waitcnt lgkmcnt(6)
	v_mfma_f32_16x16x32_bf16 v[110:113], v[178:181], v[226:229], v[110:113]
	v_mfma_f32_16x16x32_bf16 v[102:105], v[194:197], v[226:229], v[102:105]
	v_mfma_f32_16x16x32_bf16 v[82:85], v[198:201], v[226:229], v[82:85]
	buffer_load_dwordx4 v[38:41], v1, s[4:7], s23 offen sc0 nt
	s_or_b32 s23, s22, 0x18000
	s_or_b32 s22, s22, 0x1c000
	v_mfma_f32_16x16x32_bf16 v[62:65], v[202:205], v[226:229], v[62:65]
	s_waitcnt lgkmcnt(5)
	v_mfma_f32_16x16x32_bf16 v[94:97], v[178:181], v[230:233], v[94:97]
	v_mfma_f32_16x16x32_bf16 v[86:89], v[194:197], v[230:233], v[86:89]
	v_mfma_f32_16x16x32_bf16 v[70:73], v[198:201], v[230:233], v[70:73]
	buffer_load_dwordx4 v[42:45], v1, s[4:7], s23 offen sc0 nt
	v_mfma_f32_16x16x32_bf16 v[54:57], v[202:205], v[230:233], v[54:57]
	s_waitcnt lgkmcnt(4)
	v_mfma_f32_16x16x32_bf16 v[78:81], v[178:181], v[234:237], v[78:81]
	v_mfma_f32_16x16x32_bf16 v[66:69], v[194:197], v[234:237], v[66:69]
	v_mfma_f32_16x16x32_bf16 v[58:61], v[198:201], v[234:237], v[58:61]
	buffer_load_dwordx4 v[46:49], v1, s[4:7], s22 offen sc0 nt
	v_mfma_f32_16x16x32_bf16 v[50:53], v[202:205], v[234:237], v[50:53]
	s_setprio 0
	s_waitcnt lgkmcnt(0)
	s_barrier
	ds_read_b128 v[178:181], v182 offset:33792
	ds_read_b128 v[194:197], v182 offset:35840
	ds_read_b128 v[198:201], v182 offset:37888
	ds_read_b128 v[202:205], v182 offset:39936
	ds_read_b128 v[206:209], v238 offset:1024
	ds_read_b128 v[210:213], v238 offset:3072
	ds_read_b128 v[214:217], v238 offset:5120
	ds_read_b128 v[218:221], v238 offset:7168
	ds_read_b128 v[222:225], v238 offset:9216
	ds_read_b128 v[226:229], v238 offset:11264
	ds_read_b128 v[230:233], v238 offset:13312
	ds_read_b128 v[234:237], v238 offset:15360
	v_add_u32_e32 v182, s19, v190
	s_waitcnt vmcnt(11)
	ds_write_b128 v182, v[2:5] offset:32768
	s_waitcnt vmcnt(10)
	ds_write_b128 v182, v[6:9] offset:40960
	s_waitcnt vmcnt(9)
	ds_write_b128 v182, v[14:17] offset:49152
	s_waitcnt vmcnt(8)
	ds_write_b128 v182, v[26:29] offset:57344
	s_waitcnt lgkmcnt(0)
	s_barrier
	s_setprio 1
	s_lshl_b32 s21, s21, 7
	s_and_b32 s21, s21, 0x780
	s_or_b32 s21, s21, s14
	s_or_b32 s22, s21, 0x20000
	s_waitcnt lgkmcnt(11)
	v_mfma_f32_16x16x32_bf16 v[174:177], v[178:181], v[206:209], v[174:177]
	v_mfma_f32_16x16x32_bf16 v[170:173], v[194:197], v[206:209], v[170:173]
	v_mfma_f32_16x16x32_bf16 v[158:161], v[198:201], v[206:209], v[158:161]
	v_mfma_f32_16x16x32_bf16 v[142:145], v[202:205], v[206:209], v[142:145]
	s_waitcnt lgkmcnt(10)
	v_mfma_f32_16x16x32_bf16 v[166:169], v[178:181], v[210:213], v[166:169]
	v_mfma_f32_16x16x32_bf16 v[162:165], v[194:197], v[210:213], v[162:165]
	buffer_load_dwordx4 v[2:5], v188, s[0:3], s21 offen sc1
	v_mfma_f32_16x16x32_bf16 v[146:149], v[198:201], v[210:213], v[146:149]
	v_mfma_f32_16x16x32_bf16 v[122:125], v[202:205], v[210:213], v[122:125]
	s_waitcnt lgkmcnt(9)
	v_mfma_f32_16x16x32_bf16 v[154:157], v[178:181], v[214:217], v[154:157]
	v_mfma_f32_16x16x32_bf16 v[150:153], v[194:197], v[214:217], v[150:153]
	v_mfma_f32_16x16x32_bf16 v[130:133], v[198:201], v[214:217], v[130:133]
	v_mfma_f32_16x16x32_bf16 v[106:109], v[202:205], v[214:217], v[106:109]
	s_waitcnt lgkmcnt(8)
	v_mfma_f32_16x16x32_bf16 v[138:141], v[178:181], v[218:221], v[138:141]
	v_mfma_f32_16x16x32_bf16 v[134:137], v[194:197], v[218:221], v[134:137]
	buffer_load_dwordx4 v[6:9], v188, s[0:3], s22 offen sc1
	s_or_b32 s22, s21, 0x40000
	s_or_b32 s21, s21, 0x60000
	v_mfma_f32_16x16x32_bf16 v[114:117], v[198:201], v[218:221], v[114:117]
	v_mfma_f32_16x16x32_bf16 v[90:93], v[202:205], v[218:221], v[90:93]
	s_waitcnt lgkmcnt(7)
	v_mfma_f32_16x16x32_bf16 v[126:129], v[178:181], v[222:225], v[126:129]
	v_mfma_f32_16x16x32_bf16 v[118:121], v[194:197], v[222:225], v[118:121]
	v_mfma_f32_16x16x32_bf16 v[98:101], v[198:201], v[222:225], v[98:101]
	v_mfma_f32_16x16x32_bf16 v[74:77], v[202:205], v[222:225], v[74:77]
	s_waitcnt lgkmcnt(6)
	v_mfma_f32_16x16x32_bf16 v[110:113], v[178:181], v[226:229], v[110:113]
	v_mfma_f32_16x16x32_bf16 v[102:105], v[194:197], v[226:229], v[102:105]
	buffer_load_dwordx4 v[14:17], v188, s[0:3], s22 offen sc1
	v_mfma_f32_16x16x32_bf16 v[82:85], v[198:201], v[226:229], v[82:85]
	v_mfma_f32_16x16x32_bf16 v[62:65], v[202:205], v[226:229], v[62:65]
	s_waitcnt lgkmcnt(5)
	v_mfma_f32_16x16x32_bf16 v[94:97], v[178:181], v[230:233], v[94:97]
	v_mfma_f32_16x16x32_bf16 v[86:89], v[194:197], v[230:233], v[86:89]
	v_mfma_f32_16x16x32_bf16 v[70:73], v[198:201], v[230:233], v[70:73]
	v_mfma_f32_16x16x32_bf16 v[54:57], v[202:205], v[230:233], v[54:57]
	s_waitcnt lgkmcnt(4)
	v_mfma_f32_16x16x32_bf16 v[78:81], v[178:181], v[234:237], v[78:81]
	v_mfma_f32_16x16x32_bf16 v[66:69], v[194:197], v[234:237], v[66:69]
	buffer_load_dwordx4 v[26:29], v188, s[0:3], s21 offen sc1
	v_mfma_f32_16x16x32_bf16 v[58:61], v[198:201], v[234:237], v[58:61]
	v_mfma_f32_16x16x32_bf16 v[50:53], v[202:205], v[234:237], v[50:53]
	s_setprio 0
	s_and_b32 s21, s20, 15
	s_cmp_lg_u32 s21, 15
	s_cbranch_scc1 .LBB1_3
	s_and_b32 s21, s18, 32
	s_add_i32 s21, s21, s12
	s_lshl_b32 s21, s21, 6
	s_and_b32 s21, s21, 0x3f00
	v_add_lshl_u32 v182, v193, s21, 9
	v_lshl_add_u64 v[206:207], v[184:185], 0, v[182:183]
	v_add_co_u32_e32 v208, vcc, s8, v206
	v_pk_add_f32 v[176:177], v[242:243], v[176:177]
	v_addc_co_u32_e32 v209, vcc, 0, v207, vcc
	v_add_co_u32_e32 v210, vcc, s15, v206
	v_pk_add_f32 v[174:175], v[240:241], v[174:175]
	s_nop 0
	v_addc_co_u32_e32 v211, vcc, 0, v207, vcc
	v_add_co_u32_e32 v212, vcc, s9, v206
	v_pk_add_f32 v[68:69], v[246:247], v[68:69]
	v_addc_co_u32_e32 v213, vcc, 0, v207, vcc
	v_add_co_u32_e32 v214, vcc, s16, v206
	v_pk_add_f32 v[66:67], v[244:245], v[66:67]
	s_nop 0
	v_addc_co_u32_e32 v215, vcc, 0, v207, vcc
	v_add_co_u32_e32 v216, vcc, s10, v206
	v_pk_add_f32 v[168:169], v[242:243], v[168:169]
	s_nop 0
	v_addc_co_u32_e32 v217, vcc, 0, v207, vcc
	v_add_co_u32_e32 v218, vcc, s17, v206
	v_pk_add_f32 v[166:167], v[240:241], v[166:167]
	s_nop 0
	v_addc_co_u32_e32 v219, vcc, 0, v207, vcc
	v_add_co_u32_e32 v220, vcc, s11, v206
	v_pk_add_f32 v[156:157], v[242:243], v[156:157]
	s_nop 0
	v_addc_co_u32_e32 v221, vcc, 0, v207, vcc
	v_pk_add_f32 v[154:155], v[240:241], v[154:155]
	v_pk_add_f32 v[140:141], v[242:243], v[140:141]
	v_pk_add_f32 v[138:139], v[240:241], v[138:139]
	v_pk_add_f32 v[128:129], v[242:243], v[128:129]
	v_pk_add_f32 v[126:127], v[240:241], v[126:127]
	v_pk_add_f32 v[112:113], v[242:243], v[112:113]
	v_pk_add_f32 v[110:111], v[240:241], v[110:111]
	v_pk_add_f32 v[96:97], v[242:243], v[96:97]
	v_pk_add_f32 v[94:95], v[240:241], v[94:95]
	v_pk_add_f32 v[80:81], v[242:243], v[80:81]
	v_pk_add_f32 v[78:79], v[240:241], v[78:79]
	v_pk_add_f32 v[172:173], v[246:247], v[172:173]
	v_pk_add_f32 v[170:171], v[244:245], v[170:171]
	v_pk_add_f32 v[164:165], v[246:247], v[164:165]
	v_pk_add_f32 v[162:163], v[244:245], v[162:163]
	v_pk_add_f32 v[152:153], v[246:247], v[152:153]
	v_pk_add_f32 v[150:151], v[244:245], v[150:151]
	v_pk_add_f32 v[136:137], v[246:247], v[136:137]
	v_pk_add_f32 v[134:135], v[244:245], v[134:135]
	v_pk_add_f32 v[120:121], v[246:247], v[120:121]
	v_pk_add_f32 v[118:119], v[244:245], v[118:119]
	v_pk_add_f32 v[104:105], v[246:247], v[104:105]
	v_pk_add_f32 v[102:103], v[244:245], v[102:103]
	v_pk_add_f32 v[88:89], v[246:247], v[88:89]
	v_pk_add_f32 v[86:87], v[244:245], v[86:87]
	global_store_dwordx4 v[206:207], v[174:177], off
	global_store_dwordx4 v[208:209], v[166:169], off
	global_store_dwordx4 v[210:211], v[154:157], off
	global_store_dwordx4 v[212:213], v[138:141], off
	global_store_dwordx4 v[214:215], v[126:129], off
	global_store_dwordx4 v[216:217], v[110:113], off
	global_store_dwordx4 v[218:219], v[94:97], off
	global_store_dwordx4 v[220:221], v[78:81], off
	global_store_dwordx4 v[206:207], v[170:173], off offset:64
	global_store_dwordx4 v[208:209], v[162:165], off offset:64
	global_store_dwordx4 v[210:211], v[150:153], off offset:64
	global_store_dwordx4 v[212:213], v[134:137], off offset:64
	global_store_dwordx4 v[214:215], v[118:121], off offset:64
	global_store_dwordx4 v[216:217], v[102:105], off offset:64
	global_store_dwordx4 v[218:219], v[86:89], off offset:64
	global_store_dwordx4 v[220:221], v[66:69], off offset:64
	v_pk_add_f32 v[60:61], v[250:251], v[60:61]
	v_pk_add_f32 v[58:59], v[248:249], v[58:59]
	v_pk_add_f32 v[68:69], v[250:251], v[160:161]
	v_pk_add_f32 v[66:67], v[248:249], v[158:159]
	global_store_dwordx4 v[206:207], v[66:69], off offset:128
	global_store_dwordx4 v[220:221], v[58:61], off offset:128
	v_pk_add_f32 v[52:53], v[254:255], v[52:53]
	v_pk_add_f32 v[68:69], v[250:251], v[148:149]
	v_pk_add_f32 v[66:67], v[248:249], v[146:147]
	v_pk_add_f32 v[60:61], v[254:255], v[144:145]
	v_pk_add_f32 v[58:59], v[252:253], v[142:143]
	global_store_dwordx4 v[208:209], v[66:69], off offset:128
	global_store_dwordx4 v[206:207], v[58:61], off offset:192
	v_pk_add_f32 v[50:51], v[252:253], v[50:51]
	v_pk_add_f32 v[68:69], v[250:251], v[132:133]
	v_pk_add_f32 v[66:67], v[248:249], v[130:131]
	v_pk_add_f32 v[60:61], v[254:255], v[124:125]
	v_pk_add_f32 v[58:59], v[252:253], v[122:123]
	global_store_dwordx4 v[210:211], v[66:69], off offset:128
	global_store_dwordx4 v[208:209], v[58:61], off offset:192
	v_pk_add_f32 v[56:57], v[254:255], v[56:57]
	v_pk_add_f32 v[68:69], v[250:251], v[116:117]
	v_pk_add_f32 v[66:67], v[248:249], v[114:115]
	v_pk_add_f32 v[60:61], v[254:255], v[108:109]
	v_pk_add_f32 v[58:59], v[252:253], v[106:107]
	global_store_dwordx4 v[212:213], v[66:69], off offset:128
	global_store_dwordx4 v[210:211], v[58:61], off offset:192
	v_pk_add_f32 v[54:55], v[252:253], v[54:55]
	v_pk_add_f32 v[68:69], v[250:251], v[100:101]
	v_pk_add_f32 v[66:67], v[248:249], v[98:99]
	v_pk_add_f32 v[60:61], v[254:255], v[92:93]
	v_pk_add_f32 v[58:59], v[252:253], v[90:91]
	global_store_dwordx4 v[214:215], v[66:69], off offset:128
	global_store_dwordx4 v[212:213], v[58:61], off offset:192
	global_store_dwordx4 v[220:221], v[50:53], off offset:192
	v_pk_add_f32 v[68:69], v[250:251], v[84:85]
	v_pk_add_f32 v[66:67], v[248:249], v[82:83]
	v_pk_add_f32 v[60:61], v[254:255], v[76:77]
	v_pk_add_f32 v[58:59], v[252:253], v[74:75]
	global_store_dwordx4 v[216:217], v[66:69], off offset:128
	global_store_dwordx4 v[214:215], v[58:61], off offset:192
	v_mov_b32_e32 v50, 0
	v_pk_add_f32 v[68:69], v[250:251], v[72:73]
	v_pk_add_f32 v[66:67], v[248:249], v[70:71]
	v_pk_add_f32 v[60:61], v[254:255], v[64:65]
	v_pk_add_f32 v[58:59], v[252:253], v[62:63]
	global_store_dwordx4 v[218:219], v[66:69], off offset:128
	global_store_dwordx4 v[216:217], v[58:61], off offset:192
	global_store_dwordx4 v[218:219], v[54:57], off offset:192
	v_mov_b32_e32 v51, v50
	v_mov_b32_e32 v52, v50
	v_mov_b32_e32 v53, v50
	v_mov_b32_e32 v58, v50
	v_mov_b32_e32 v59, v50
	v_mov_b32_e32 v60, v50
	v_mov_b32_e32 v61, v50
	v_mov_b32_e32 v66, v50
	v_mov_b32_e32 v67, v50
	v_mov_b32_e32 v68, v50
	v_mov_b32_e32 v69, v50
	v_mov_b32_e32 v78, v50
	v_mov_b32_e32 v79, v50
	v_mov_b32_e32 v80, v50
	v_mov_b32_e32 v81, v50
	v_mov_b32_e32 v54, v50
	v_mov_b32_e32 v55, v50
	v_mov_b32_e32 v56, v50
	v_mov_b32_e32 v57, v50
	v_mov_b32_e32 v70, v50
	v_mov_b32_e32 v71, v50
	v_mov_b32_e32 v72, v50
	v_mov_b32_e32 v73, v50
	v_mov_b32_e32 v86, v50
	v_mov_b32_e32 v87, v50
	v_mov_b32_e32 v88, v50
	v_mov_b32_e32 v89, v50
	v_mov_b32_e32 v94, v50
	v_mov_b32_e32 v95, v50
	v_mov_b32_e32 v96, v50
	v_mov_b32_e32 v97, v50
	v_mov_b32_e32 v62, v50
	v_mov_b32_e32 v63, v50
	v_mov_b32_e32 v64, v50
	v_mov_b32_e32 v65, v50
	v_mov_b32_e32 v82, v50
	v_mov_b32_e32 v83, v50
	v_mov_b32_e32 v84, v50
	v_mov_b32_e32 v85, v50
	v_mov_b32_e32 v102, v50
	v_mov_b32_e32 v103, v50
	v_mov_b32_e32 v104, v50
	v_mov_b32_e32 v105, v50
	v_mov_b32_e32 v110, v50
	v_mov_b32_e32 v111, v50
	v_mov_b32_e32 v112, v50
	v_mov_b32_e32 v113, v50
	v_mov_b32_e32 v74, v50
	v_mov_b32_e32 v75, v50
	v_mov_b32_e32 v76, v50
	v_mov_b32_e32 v77, v50
	v_mov_b32_e32 v98, v50
	v_mov_b32_e32 v99, v50
	v_mov_b32_e32 v100, v50
	v_mov_b32_e32 v101, v50
	v_mov_b32_e32 v118, v50
	v_mov_b32_e32 v119, v50
	v_mov_b32_e32 v120, v50
	v_mov_b32_e32 v121, v50
	v_mov_b32_e32 v126, v50
	v_mov_b32_e32 v127, v50
	v_mov_b32_e32 v128, v50
	v_mov_b32_e32 v129, v50
	v_mov_b32_e32 v90, v50
	v_mov_b32_e32 v91, v50
	v_mov_b32_e32 v92, v50
	v_mov_b32_e32 v93, v50
	v_mov_b32_e32 v114, v50
	v_mov_b32_e32 v115, v50
	v_mov_b32_e32 v116, v50
	v_mov_b32_e32 v117, v50
	v_mov_b32_e32 v134, v50
	v_mov_b32_e32 v135, v50
	v_mov_b32_e32 v136, v50
	v_mov_b32_e32 v137, v50
	v_mov_b32_e32 v138, v50
	v_mov_b32_e32 v139, v50
	v_mov_b32_e32 v140, v50
	v_mov_b32_e32 v141, v50
	v_mov_b32_e32 v106, v50
	v_mov_b32_e32 v107, v50
	v_mov_b32_e32 v108, v50
	v_mov_b32_e32 v109, v50
	v_mov_b32_e32 v130, v50
	v_mov_b32_e32 v131, v50
	v_mov_b32_e32 v132, v50
	v_mov_b32_e32 v133, v50
	v_mov_b32_e32 v150, v50
	v_mov_b32_e32 v151, v50
	v_mov_b32_e32 v152, v50
	v_mov_b32_e32 v153, v50
	v_mov_b32_e32 v154, v50
	v_mov_b32_e32 v155, v50
	v_mov_b32_e32 v156, v50
	v_mov_b32_e32 v157, v50
	v_mov_b32_e32 v122, v50
	v_mov_b32_e32 v123, v50
	v_mov_b32_e32 v124, v50
	v_mov_b32_e32 v125, v50
	v_mov_b32_e32 v146, v50
	v_mov_b32_e32 v147, v50
	v_mov_b32_e32 v148, v50
	v_mov_b32_e32 v149, v50
	v_mov_b32_e32 v162, v50
	v_mov_b32_e32 v163, v50
	v_mov_b32_e32 v164, v50
	v_mov_b32_e32 v165, v50
	v_mov_b32_e32 v166, v50
	v_mov_b32_e32 v167, v50
	v_mov_b32_e32 v168, v50
	v_mov_b32_e32 v169, v50
	v_mov_b32_e32 v142, v50
	v_mov_b32_e32 v143, v50
	v_mov_b32_e32 v144, v50
	v_mov_b32_e32 v145, v50
	v_mov_b32_e32 v158, v50
	v_mov_b32_e32 v159, v50
	v_mov_b32_e32 v160, v50
	v_mov_b32_e32 v161, v50
	v_mov_b32_e32 v170, v50
	v_mov_b32_e32 v171, v50
	v_mov_b32_e32 v172, v50
	v_mov_b32_e32 v173, v50
	v_mov_b32_e32 v174, v50
	v_mov_b32_e32 v175, v50
	v_mov_b32_e32 v176, v50
	v_mov_b32_e32 v177, v50
	s_branch .Lpd_tail

.Lt30:
	v_add_u32_e32 v182, s19, v191
	v_add_u32_e32 v238, s19, v192
	ds_read_b128 v[178:181], v182 offset:32768
	ds_read_b128 v[194:197], v182 offset:34816
	ds_read_b128 v[198:201], v182 offset:36864
	ds_read_b128 v[202:205], v182 offset:38912
	ds_read_b128 v[206:209], v238
	ds_read_b128 v[210:213], v238 offset:2048
	ds_read_b128 v[214:217], v238 offset:4096
	ds_read_b128 v[218:221], v238 offset:6144
	ds_read_b128 v[222:225], v238 offset:8192
	ds_read_b128 v[226:229], v238 offset:10240
	ds_read_b128 v[230:233], v238 offset:12288
	ds_read_b128 v[234:237], v238 offset:14336
	s_min_u32 s21, s20, 29
	s_xor_b32 s19, s19, 0x10000
	v_add_u32_e32 v239, s19, v189
	s_waitcnt vmcnt(11)
	v_cvt_pk_bf16_f32 v13, v12, v13
	v_cvt_pk_bf16_f32 v12, v10, v11
	s_waitcnt vmcnt(10)
	v_cvt_pk_bf16_f32 v11, v20, v21
	v_cvt_pk_bf16_f32 v10, v18, v19
	ds_write2st64_b64 v239, v[12:13], v[10:11] offset1:8
	s_waitcnt vmcnt(9)
	v_cvt_pk_bf16_f32 v11, v24, v25
	v_cvt_pk_bf16_f32 v10, v22, v23
	s_waitcnt vmcnt(8)
	v_cvt_pk_bf16_f32 v13, v32, v33
	v_cvt_pk_bf16_f32 v12, v30, v31
	ds_write2st64_b64 v239, v[10:11], v[12:13] offset0:16 offset1:24
	s_waitcnt vmcnt(7)
	v_cvt_pk_bf16_f32 v11, v36, v37
	v_cvt_pk_bf16_f32 v10, v34, v35
	s_waitcnt vmcnt(6)
	v_cvt_pk_bf16_f32 v13, v40, v41
	v_cvt_pk_bf16_f32 v12, v38, v39
	ds_write2st64_b64 v239, v[10:11], v[12:13] offset0:32 offset1:40
	s_waitcnt vmcnt(5)
	v_cvt_pk_bf16_f32 v11, v44, v45
	v_cvt_pk_bf16_f32 v10, v42, v43
	s_waitcnt vmcnt(4)
	v_cvt_pk_bf16_f32 v13, v48, v49
	v_cvt_pk_bf16_f32 v12, v46, v47
	ds_write2st64_b64 v239, v[10:11], v[12:13] offset0:48 offset1:56
	s_waitcnt lgkmcnt(0)
	s_add_i32 s21, s21, 2
	s_barrier
	s_setprio 1
	s_lshl_b32 s22, s21, 1
	s_and_b32 s22, s22, 0x60
	s_add_i32 s22, s22, s12
	s_lshl_b32 s22, s22, 6
	s_and_b32 s22, s22, 0x3f00
	s_or_b32 s22, s22, s13
	s_lshl_b32 s23, s21, 23
	s_lshl_b32 s22, s22, 9
	s_and_b32 s23, s23, 0x7000000
	s_or_b32 s22, s22, s23
	s_lshl_b32 s23, s21, 8
	s_and_b32 s23, s23, 0x100
	s_or_b32 s22, s22, s23
	s_or_b32 s23, s22, 0x4000
	s_waitcnt lgkmcnt(11)
	v_mfma_f32_16x16x32_bf16 v[174:177], v[178:181], v[206:209], v[174:177]
	v_mfma_f32_16x16x32_bf16 v[170:173], v[194:197], v[206:209], v[170:173]
	v_mfma_f32_16x16x32_bf16 v[158:161], v[198:201], v[206:209], v[158:161]
	v_mfma_f32_16x16x32_bf16 v[142:145], v[202:205], v[206:209], v[142:145]
	s_waitcnt lgkmcnt(10)
	v_mfma_f32_16x16x32_bf16 v[166:169], v[178:181], v[210:213], v[166:169]
	v_mfma_f32_16x16x32_bf16 v[162:165], v[194:197], v[210:213], v[162:165]
	v_mfma_f32_16x16x32_bf16 v[146:149], v[198:201], v[210:213], v[146:149]
	s_or_b32 s23, s22, 0x8000
	v_mfma_f32_16x16x32_bf16 v[122:125], v[202:205], v[210:213], v[122:125]
	s_waitcnt lgkmcnt(9)
	v_mfma_f32_16x16x32_bf16 v[154:157], v[178:181], v[214:217], v[154:157]
	v_mfma_f32_16x16x32_bf16 v[150:153], v[194:197], v[214:217], v[150:153]
	v_mfma_f32_16x16x32_bf16 v[130:133], v[198:201], v[214:217], v[130:133]
	s_or_b32 s23, s22, 0xc000
	v_mfma_f32_16x16x32_bf16 v[106:109], v[202:205], v[214:217], v[106:109]
	s_waitcnt lgkmcnt(8)
	v_mfma_f32_16x16x32_bf16 v[138:141], v[178:181], v[218:221], v[138:141]
	v_mfma_f32_16x16x32_bf16 v[134:137], v[194:197], v[218:221], v[134:137]
	v_mfma_f32_16x16x32_bf16 v[114:117], v[198:201], v[218:221], v[114:117]
	s_or_b32 s23, s22, 0x10000
	v_mfma_f32_16x16x32_bf16 v[90:93], v[202:205], v[218:221], v[90:93]
	s_waitcnt lgkmcnt(7)
	v_mfma_f32_16x16x32_bf16 v[126:129], v[178:181], v[222:225], v[126:129]
	v_mfma_f32_16x16x32_bf16 v[118:121], v[194:197], v[222:225], v[118:121]
	v_mfma_f32_16x16x32_bf16 v[98:101], v[198:201], v[222:225], v[98:101]
	s_or_b32 s23, s22, 0x14000
	v_mfma_f32_16x16x32_bf16 v[74:77], v[202:205], v[222:225], v[74:77]
	s_waitcnt lgkmcnt(6)
	v_mfma_f32_16x16x32_bf16 v[110:113], v[178:181], v[226:229], v[110:113]
	v_mfma_f32_16x16x32_bf16 v[102:105], v[194:197], v[226:229], v[102:105]
	v_mfma_f32_16x16x32_bf16 v[82:85], v[198:201], v[226:229], v[82:85]
	s_or_b32 s23, s22, 0x18000
	s_or_b32 s22, s22, 0x1c000
	v_mfma_f32_16x16x32_bf16 v[62:65], v[202:205], v[226:229], v[62:65]
	s_waitcnt lgkmcnt(5)
	v_mfma_f32_16x16x32_bf16 v[94:97], v[178:181], v[230:233], v[94:97]
	v_mfma_f32_16x16x32_bf16 v[86:89], v[194:197], v[230:233], v[86:89]
	v_mfma_f32_16x16x32_bf16 v[70:73], v[198:201], v[230:233], v[70:73]
	v_mfma_f32_16x16x32_bf16 v[54:57], v[202:205], v[230:233], v[54:57]
	s_waitcnt lgkmcnt(4)
	v_mfma_f32_16x16x32_bf16 v[78:81], v[178:181], v[234:237], v[78:81]
	v_mfma_f32_16x16x32_bf16 v[66:69], v[194:197], v[234:237], v[66:69]
	v_mfma_f32_16x16x32_bf16 v[58:61], v[198:201], v[234:237], v[58:61]
	v_mfma_f32_16x16x32_bf16 v[50:53], v[202:205], v[234:237], v[50:53]
	s_setprio 0
	s_waitcnt lgkmcnt(0)
	s_barrier
	ds_read_b128 v[178:181], v182 offset:33792
	ds_read_b128 v[194:197], v182 offset:35840
	ds_read_b128 v[198:201], v182 offset:37888
	ds_read_b128 v[202:205], v182 offset:39936
	ds_read_b128 v[206:209], v238 offset:1024
	ds_read_b128 v[210:213], v238 offset:3072
	ds_read_b128 v[214:217], v238 offset:5120
	ds_read_b128 v[218:221], v238 offset:7168
	ds_read_b128 v[222:225], v238 offset:9216
	ds_read_b128 v[226:229], v238 offset:11264
	ds_read_b128 v[230:233], v238 offset:13312
	ds_read_b128 v[234:237], v238 offset:15360
	v_add_u32_e32 v182, s19, v190
	s_waitcnt vmcnt(3)
	ds_write_b128 v182, v[2:5] offset:32768
	s_waitcnt vmcnt(2)
	ds_write_b128 v182, v[6:9] offset:40960
	s_waitcnt vmcnt(1)
	ds_write_b128 v182, v[14:17] offset:49152
	s_waitcnt vmcnt(0)
	ds_write_b128 v182, v[26:29] offset:57344
	s_waitcnt lgkmcnt(0)
	s_barrier
	s_setprio 1
	s_lshl_b32 s21, s21, 7
	s_and_b32 s21, s21, 0x780
	s_or_b32 s21, s21, s14
	s_or_b32 s22, s21, 0x20000
	s_waitcnt lgkmcnt(11)
	v_mfma_f32_16x16x32_bf16 v[174:177], v[178:181], v[206:209], v[174:177]
	v_mfma_f32_16x16x32_bf16 v[170:173], v[194:197], v[206:209], v[170:173]
	v_mfma_f32_16x16x32_bf16 v[158:161], v[198:201], v[206:209], v[158:161]
	v_mfma_f32_16x16x32_bf16 v[142:145], v[202:205], v[206:209], v[142:145]
	s_waitcnt lgkmcnt(10)
	v_mfma_f32_16x16x32_bf16 v[166:169], v[178:181], v[210:213], v[166:169]
	v_mfma_f32_16x16x32_bf16 v[162:165], v[194:197], v[210:213], v[162:165]
	v_mfma_f32_16x16x32_bf16 v[146:149], v[198:201], v[210:213], v[146:149]
	v_mfma_f32_16x16x32_bf16 v[122:125], v[202:205], v[210:213], v[122:125]
	s_waitcnt lgkmcnt(9)
	v_mfma_f32_16x16x32_bf16 v[154:157], v[178:181], v[214:217], v[154:157]
	v_mfma_f32_16x16x32_bf16 v[150:153], v[194:197], v[214:217], v[150:153]
	v_mfma_f32_16x16x32_bf16 v[130:133], v[198:201], v[214:217], v[130:133]
	v_mfma_f32_16x16x32_bf16 v[106:109], v[202:205], v[214:217], v[106:109]
	s_waitcnt lgkmcnt(8)
	v_mfma_f32_16x16x32_bf16 v[138:141], v[178:181], v[218:221], v[138:141]
	v_mfma_f32_16x16x32_bf16 v[134:137], v[194:197], v[218:221], v[134:137]
	s_or_b32 s22, s21, 0x40000
	s_or_b32 s21, s21, 0x60000
	v_mfma_f32_16x16x32_bf16 v[114:117], v[198:201], v[218:221], v[114:117]
	v_mfma_f32_16x16x32_bf16 v[90:93], v[202:205], v[218:221], v[90:93]
	s_waitcnt lgkmcnt(7)
	v_mfma_f32_16x16x32_bf16 v[126:129], v[178:181], v[222:225], v[126:129]
	v_mfma_f32_16x16x32_bf16 v[118:121], v[194:197], v[222:225], v[118:121]
	v_mfma_f32_16x16x32_bf16 v[98:101], v[198:201], v[222:225], v[98:101]
	v_mfma_f32_16x16x32_bf16 v[74:77], v[202:205], v[222:225], v[74:77]
	s_waitcnt lgkmcnt(6)
	v_mfma_f32_16x16x32_bf16 v[110:113], v[178:181], v[226:229], v[110:113]
	v_mfma_f32_16x16x32_bf16 v[102:105], v[194:197], v[226:229], v[102:105]
	v_mfma_f32_16x16x32_bf16 v[82:85], v[198:201], v[226:229], v[82:85]
	v_mfma_f32_16x16x32_bf16 v[62:65], v[202:205], v[226:229], v[62:65]
	s_waitcnt lgkmcnt(5)
	v_mfma_f32_16x16x32_bf16 v[94:97], v[178:181], v[230:233], v[94:97]
	v_mfma_f32_16x16x32_bf16 v[86:89], v[194:197], v[230:233], v[86:89]
	v_mfma_f32_16x16x32_bf16 v[70:73], v[198:201], v[230:233], v[70:73]
	v_mfma_f32_16x16x32_bf16 v[54:57], v[202:205], v[230:233], v[54:57]
	s_waitcnt lgkmcnt(4)
	v_mfma_f32_16x16x32_bf16 v[78:81], v[178:181], v[234:237], v[78:81]
	v_mfma_f32_16x16x32_bf16 v[66:69], v[194:197], v[234:237], v[66:69]
	v_mfma_f32_16x16x32_bf16 v[58:61], v[198:201], v[234:237], v[58:61]
	v_mfma_f32_16x16x32_bf16 v[50:53], v[202:205], v[234:237], v[50:53]
	s_setprio 0
	s_waitcnt lgkmcnt(0)
	s_barrier
	s_add_i32 s20, s20, 1
	s_add_i32 s18, s18, 2
	v_add_u32_e32 v182, s19, v191
	v_add_u32_e32 v238, s19, v192
	ds_read_b128 v[178:181], v182 offset:32768
	ds_read_b128 v[194:197], v182 offset:34816
	ds_read_b128 v[198:201], v182 offset:36864
	ds_read_b128 v[202:205], v182 offset:38912
	ds_read_b128 v[206:209], v238
	ds_read_b128 v[210:213], v238 offset:2048
	ds_read_b128 v[214:217], v238 offset:4096
	ds_read_b128 v[218:221], v238 offset:6144
	ds_read_b128 v[222:225], v238 offset:8192
	ds_read_b128 v[226:229], v238 offset:10240
	ds_read_b128 v[230:233], v238 offset:12288
	ds_read_b128 v[234:237], v238 offset:14336
	s_min_u32 s21, s20, 29
	s_xor_b32 s19, s19, 0x10000
	v_add_u32_e32 v239, s19, v189
	s_waitcnt lgkmcnt(0)
	s_add_i32 s21, s21, 2
	s_barrier
	s_setprio 1
	s_lshl_b32 s22, s21, 1
	s_and_b32 s22, s22, 0x60
	s_add_i32 s22, s22, s12
	s_lshl_b32 s22, s22, 6
	s_and_b32 s22, s22, 0x3f00
	s_or_b32 s22, s22, s13
	s_lshl_b32 s23, s21, 23
	s_lshl_b32 s22, s22, 9
	s_and_b32 s23, s23, 0x7000000
	s_or_b32 s22, s22, s23
	s_lshl_b32 s23, s21, 8
	s_and_b32 s23, s23, 0x100
	s_or_b32 s22, s22, s23
	s_or_b32 s23, s22, 0x4000
	s_waitcnt lgkmcnt(11)
	v_mfma_f32_16x16x32_bf16 v[174:177], v[178:181], v[206:209], v[174:177]
	v_mfma_f32_16x16x32_bf16 v[170:173], v[194:197], v[206:209], v[170:173]
	v_mfma_f32_16x16x32_bf16 v[158:161], v[198:201], v[206:209], v[158:161]
	v_mfma_f32_16x16x32_bf16 v[142:145], v[202:205], v[206:209], v[142:145]
	s_waitcnt lgkmcnt(10)
	v_mfma_f32_16x16x32_bf16 v[166:169], v[178:181], v[210:213], v[166:169]
	v_mfma_f32_16x16x32_bf16 v[162:165], v[194:197], v[210:213], v[162:165]
	v_mfma_f32_16x16x32_bf16 v[146:149], v[198:201], v[210:213], v[146:149]
	s_or_b32 s23, s22, 0x8000
	v_mfma_f32_16x16x32_bf16 v[122:125], v[202:205], v[210:213], v[122:125]
	s_waitcnt lgkmcnt(9)
	v_mfma_f32_16x16x32_bf16 v[154:157], v[178:181], v[214:217], v[154:157]
	v_mfma_f32_16x16x32_bf16 v[150:153], v[194:197], v[214:217], v[150:153]
	v_mfma_f32_16x16x32_bf16 v[130:133], v[198:201], v[214:217], v[130:133]
	s_or_b32 s23, s22, 0xc000
	v_mfma_f32_16x16x32_bf16 v[106:109], v[202:205], v[214:217], v[106:109]
	s_waitcnt lgkmcnt(8)
	v_mfma_f32_16x16x32_bf16 v[138:141], v[178:181], v[218:221], v[138:141]
	v_mfma_f32_16x16x32_bf16 v[134:137], v[194:197], v[218:221], v[134:137]
	v_mfma_f32_16x16x32_bf16 v[114:117], v[198:201], v[218:221], v[114:117]
	s_or_b32 s23, s22, 0x10000
	v_mfma_f32_16x16x32_bf16 v[90:93], v[202:205], v[218:221], v[90:93]
	s_waitcnt lgkmcnt(7)
	v_mfma_f32_16x16x32_bf16 v[126:129], v[178:181], v[222:225], v[126:129]
	v_mfma_f32_16x16x32_bf16 v[118:121], v[194:197], v[222:225], v[118:121]
	v_mfma_f32_16x16x32_bf16 v[98:101], v[198:201], v[222:225], v[98:101]
	s_or_b32 s23, s22, 0x14000
	v_mfma_f32_16x16x32_bf16 v[74:77], v[202:205], v[222:225], v[74:77]
	s_waitcnt lgkmcnt(6)
	v_mfma_f32_16x16x32_bf16 v[110:113], v[178:181], v[226:229], v[110:113]
	v_mfma_f32_16x16x32_bf16 v[102:105], v[194:197], v[226:229], v[102:105]
	v_mfma_f32_16x16x32_bf16 v[82:85], v[198:201], v[226:229], v[82:85]
	s_or_b32 s23, s22, 0x18000
	s_or_b32 s22, s22, 0x1c000
	v_mfma_f32_16x16x32_bf16 v[62:65], v[202:205], v[226:229], v[62:65]
	s_waitcnt lgkmcnt(5)
	v_mfma_f32_16x16x32_bf16 v[94:97], v[178:181], v[230:233], v[94:97]
	v_mfma_f32_16x16x32_bf16 v[86:89], v[194:197], v[230:233], v[86:89]
	v_mfma_f32_16x16x32_bf16 v[70:73], v[198:201], v[230:233], v[70:73]
	v_mfma_f32_16x16x32_bf16 v[54:57], v[202:205], v[230:233], v[54:57]
	s_waitcnt lgkmcnt(4)
	v_mfma_f32_16x16x32_bf16 v[78:81], v[178:181], v[234:237], v[78:81]
	v_mfma_f32_16x16x32_bf16 v[66:69], v[194:197], v[234:237], v[66:69]
	v_mfma_f32_16x16x32_bf16 v[58:61], v[198:201], v[234:237], v[58:61]
	v_mfma_f32_16x16x32_bf16 v[50:53], v[202:205], v[234:237], v[50:53]
	s_setprio 0
	s_waitcnt lgkmcnt(0)
	s_barrier
	ds_read_b128 v[178:181], v182 offset:33792
	ds_read_b128 v[194:197], v182 offset:35840
	ds_read_b128 v[198:201], v182 offset:37888
	ds_read_b128 v[202:205], v182 offset:39936
	ds_read_b128 v[206:209], v238 offset:1024
	ds_read_b128 v[210:213], v238 offset:3072
	ds_read_b128 v[214:217], v238 offset:5120
	ds_read_b128 v[218:221], v238 offset:7168
	ds_read_b128 v[222:225], v238 offset:9216
	ds_read_b128 v[226:229], v238 offset:11264
	ds_read_b128 v[230:233], v238 offset:13312
	ds_read_b128 v[234:237], v238 offset:15360
	s_waitcnt lgkmcnt(0)
	s_barrier
	s_setprio 1
	s_lshl_b32 s21, s21, 7
	s_and_b32 s21, s21, 0x780
	s_or_b32 s21, s21, s14
	s_or_b32 s22, s21, 0x20000
	s_waitcnt lgkmcnt(11)
	v_mfma_f32_16x16x32_bf16 v[174:177], v[178:181], v[206:209], v[174:177]
	v_mfma_f32_16x16x32_bf16 v[170:173], v[194:197], v[206:209], v[170:173]
	v_mfma_f32_16x16x32_bf16 v[158:161], v[198:201], v[206:209], v[158:161]
	v_mfma_f32_16x16x32_bf16 v[142:145], v[202:205], v[206:209], v[142:145]
	s_waitcnt lgkmcnt(10)
	v_mfma_f32_16x16x32_bf16 v[166:169], v[178:181], v[210:213], v[166:169]
	v_mfma_f32_16x16x32_bf16 v[162:165], v[194:197], v[210:213], v[162:165]
	v_mfma_f32_16x16x32_bf16 v[146:149], v[198:201], v[210:213], v[146:149]
	v_mfma_f32_16x16x32_bf16 v[122:125], v[202:205], v[210:213], v[122:125]
	s_waitcnt lgkmcnt(9)
	v_mfma_f32_16x16x32_bf16 v[154:157], v[178:181], v[214:217], v[154:157]
	v_mfma_f32_16x16x32_bf16 v[150:153], v[194:197], v[214:217], v[150:153]
	v_mfma_f32_16x16x32_bf16 v[130:133], v[198:201], v[214:217], v[130:133]
	v_mfma_f32_16x16x32_bf16 v[106:109], v[202:205], v[214:217], v[106:109]
	s_waitcnt lgkmcnt(8)
	v_mfma_f32_16x16x32_bf16 v[138:141], v[178:181], v[218:221], v[138:141]
	v_mfma_f32_16x16x32_bf16 v[134:137], v[194:197], v[218:221], v[134:137]
	s_or_b32 s22, s21, 0x40000
	s_or_b32 s21, s21, 0x60000
	v_mfma_f32_16x16x32_bf16 v[114:117], v[198:201], v[218:221], v[114:117]
	v_mfma_f32_16x16x32_bf16 v[90:93], v[202:205], v[218:221], v[90:93]
	s_waitcnt lgkmcnt(7)
	v_mfma_f32_16x16x32_bf16 v[126:129], v[178:181], v[222:225], v[126:129]
	v_mfma_f32_16x16x32_bf16 v[118:121], v[194:197], v[222:225], v[118:121]
	v_mfma_f32_16x16x32_bf16 v[98:101], v[198:201], v[222:225], v[98:101]
	v_mfma_f32_16x16x32_bf16 v[74:77], v[202:205], v[222:225], v[74:77]
	s_waitcnt lgkmcnt(6)
	v_mfma_f32_16x16x32_bf16 v[110:113], v[178:181], v[226:229], v[110:113]
	v_mfma_f32_16x16x32_bf16 v[102:105], v[194:197], v[226:229], v[102:105]
	v_mfma_f32_16x16x32_bf16 v[82:85], v[198:201], v[226:229], v[82:85]
	v_mfma_f32_16x16x32_bf16 v[62:65], v[202:205], v[226:229], v[62:65]
	s_waitcnt lgkmcnt(5)
	v_mfma_f32_16x16x32_bf16 v[94:97], v[178:181], v[230:233], v[94:97]
	v_mfma_f32_16x16x32_bf16 v[86:89], v[194:197], v[230:233], v[86:89]
	v_mfma_f32_16x16x32_bf16 v[70:73], v[198:201], v[230:233], v[70:73]
	v_mfma_f32_16x16x32_bf16 v[54:57], v[202:205], v[230:233], v[54:57]
	s_waitcnt lgkmcnt(4)
	v_mfma_f32_16x16x32_bf16 v[78:81], v[178:181], v[234:237], v[78:81]
	v_mfma_f32_16x16x32_bf16 v[66:69], v[194:197], v[234:237], v[66:69]
	v_mfma_f32_16x16x32_bf16 v[58:61], v[198:201], v[234:237], v[58:61]
	v_mfma_f32_16x16x32_bf16 v[50:53], v[202:205], v[234:237], v[50:53]
	s_setprio 0
	s_and_b32 s21, s18, 32
	s_add_i32 s21, s21, s12
	s_lshl_b32 s21, s21, 6
	s_and_b32 s21, s21, 0x3f00
	v_add_lshl_u32 v182, v193, s21, 9
	v_lshl_add_u64 v[206:207], v[184:185], 0, v[182:183]
	v_add_co_u32_e32 v208, vcc, s8, v206
	v_pk_add_f32 v[176:177], v[242:243], v[176:177]
	v_addc_co_u32_e32 v209, vcc, 0, v207, vcc
	v_add_co_u32_e32 v210, vcc, s15, v206
	v_pk_add_f32 v[174:175], v[240:241], v[174:175]
	s_nop 0
	v_addc_co_u32_e32 v211, vcc, 0, v207, vcc
	v_add_co_u32_e32 v212, vcc, s9, v206
	v_pk_add_f32 v[68:69], v[246:247], v[68:69]
	v_addc_co_u32_e32 v213, vcc, 0, v207, vcc
	v_add_co_u32_e32 v214, vcc, s16, v206
	v_pk_add_f32 v[66:67], v[244:245], v[66:67]
	s_nop 0
	v_addc_co_u32_e32 v215, vcc, 0, v207, vcc
	v_add_co_u32_e32 v216, vcc, s10, v206
	v_pk_add_f32 v[168:169], v[242:243], v[168:169]
	s_nop 0
	v_addc_co_u32_e32 v217, vcc, 0, v207, vcc
	v_add_co_u32_e32 v218, vcc, s17, v206
	v_pk_add_f32 v[166:167], v[240:241], v[166:167]
	s_nop 0
	v_addc_co_u32_e32 v219, vcc, 0, v207, vcc
	v_add_co_u32_e32 v220, vcc, s11, v206
	v_pk_add_f32 v[156:157], v[242:243], v[156:157]
	s_nop 0
	v_addc_co_u32_e32 v221, vcc, 0, v207, vcc
	v_pk_add_f32 v[154:155], v[240:241], v[154:155]
	v_pk_add_f32 v[140:141], v[242:243], v[140:141]
	v_pk_add_f32 v[138:139], v[240:241], v[138:139]
	v_pk_add_f32 v[128:129], v[242:243], v[128:129]
	v_pk_add_f32 v[126:127], v[240:241], v[126:127]
	v_pk_add_f32 v[112:113], v[242:243], v[112:113]
	v_pk_add_f32 v[110:111], v[240:241], v[110:111]
	v_pk_add_f32 v[96:97], v[242:243], v[96:97]
	v_pk_add_f32 v[94:95], v[240:241], v[94:95]
	v_pk_add_f32 v[80:81], v[242:243], v[80:81]
	v_pk_add_f32 v[78:79], v[240:241], v[78:79]
	v_pk_add_f32 v[172:173], v[246:247], v[172:173]
	v_pk_add_f32 v[170:171], v[244:245], v[170:171]
	v_pk_add_f32 v[164:165], v[246:247], v[164:165]
	v_pk_add_f32 v[162:163], v[244:245], v[162:163]
	v_pk_add_f32 v[152:153], v[246:247], v[152:153]
	v_pk_add_f32 v[150:151], v[244:245], v[150:151]
	v_pk_add_f32 v[136:137], v[246:247], v[136:137]
	v_pk_add_f32 v[134:135], v[244:245], v[134:135]
	v_pk_add_f32 v[120:121], v[246:247], v[120:121]
	v_pk_add_f32 v[118:119], v[244:245], v[118:119]
	v_pk_add_f32 v[104:105], v[246:247], v[104:105]
	v_pk_add_f32 v[102:103], v[244:245], v[102:103]
	v_pk_add_f32 v[88:89], v[246:247], v[88:89]
	v_pk_add_f32 v[86:87], v[244:245], v[86:87]
	global_store_dwordx4 v[206:207], v[174:177], off
	global_store_dwordx4 v[208:209], v[166:169], off
	global_store_dwordx4 v[210:211], v[154:157], off
	global_store_dwordx4 v[212:213], v[138:141], off
	global_store_dwordx4 v[214:215], v[126:129], off
	global_store_dwordx4 v[216:217], v[110:113], off
	global_store_dwordx4 v[218:219], v[94:97], off
	global_store_dwordx4 v[220:221], v[78:81], off
	global_store_dwordx4 v[206:207], v[170:173], off offset:64
	global_store_dwordx4 v[208:209], v[162:165], off offset:64
	global_store_dwordx4 v[210:211], v[150:153], off offset:64
	global_store_dwordx4 v[212:213], v[134:137], off offset:64
	global_store_dwordx4 v[214:215], v[118:121], off offset:64
	global_store_dwordx4 v[216:217], v[102:105], off offset:64
	global_store_dwordx4 v[218:219], v[86:89], off offset:64
	global_store_dwordx4 v[220:221], v[66:69], off offset:64
	v_pk_add_f32 v[60:61], v[250:251], v[60:61]
	v_pk_add_f32 v[58:59], v[248:249], v[58:59]
	v_pk_add_f32 v[68:69], v[250:251], v[160:161]
	v_pk_add_f32 v[66:67], v[248:249], v[158:159]
	global_store_dwordx4 v[206:207], v[66:69], off offset:128
	global_store_dwordx4 v[220:221], v[58:61], off offset:128
	v_pk_add_f32 v[52:53], v[254:255], v[52:53]
	v_pk_add_f32 v[68:69], v[250:251], v[148:149]
	v_pk_add_f32 v[66:67], v[248:249], v[146:147]
	v_pk_add_f32 v[60:61], v[254:255], v[144:145]
	v_pk_add_f32 v[58:59], v[252:253], v[142:143]
	global_store_dwordx4 v[208:209], v[66:69], off offset:128
	global_store_dwordx4 v[206:207], v[58:61], off offset:192
	v_pk_add_f32 v[50:51], v[252:253], v[50:51]
	v_pk_add_f32 v[68:69], v[250:251], v[132:133]
	v_pk_add_f32 v[66:67], v[248:249], v[130:131]
	v_pk_add_f32 v[60:61], v[254:255], v[124:125]
	v_pk_add_f32 v[58:59], v[252:253], v[122:123]
	global_store_dwordx4 v[210:211], v[66:69], off offset:128
	global_store_dwordx4 v[208:209], v[58:61], off offset:192
	v_pk_add_f32 v[56:57], v[254:255], v[56:57]
	v_pk_add_f32 v[68:69], v[250:251], v[116:117]
	v_pk_add_f32 v[66:67], v[248:249], v[114:115]
	v_pk_add_f32 v[60:61], v[254:255], v[108:109]
	v_pk_add_f32 v[58:59], v[252:253], v[106:107]
	global_store_dwordx4 v[212:213], v[66:69], off offset:128
	global_store_dwordx4 v[210:211], v[58:61], off offset:192
	v_pk_add_f32 v[54:55], v[252:253], v[54:55]
	v_pk_add_f32 v[68:69], v[250:251], v[100:101]
	v_pk_add_f32 v[66:67], v[248:249], v[98:99]
	v_pk_add_f32 v[60:61], v[254:255], v[92:93]
	v_pk_add_f32 v[58:59], v[252:253], v[90:91]
	global_store_dwordx4 v[214:215], v[66:69], off offset:128
	global_store_dwordx4 v[212:213], v[58:61], off offset:192
	global_store_dwordx4 v[220:221], v[50:53], off offset:192
	v_pk_add_f32 v[68:69], v[250:251], v[84:85]
	v_pk_add_f32 v[66:67], v[248:249], v[82:83]
	v_pk_add_f32 v[60:61], v[254:255], v[76:77]
	v_pk_add_f32 v[58:59], v[252:253], v[74:75]
	global_store_dwordx4 v[216:217], v[66:69], off offset:128
	global_store_dwordx4 v[214:215], v[58:61], off offset:192
	v_pk_add_f32 v[68:69], v[250:251], v[72:73]
	v_pk_add_f32 v[66:67], v[248:249], v[70:71]
	v_pk_add_f32 v[60:61], v[254:255], v[64:65]
	v_pk_add_f32 v[58:59], v[252:253], v[62:63]
	global_store_dwordx4 v[218:219], v[66:69], off offset:128
	global_store_dwordx4 v[216:217], v[58:61], off offset:192
	global_store_dwordx4 v[218:219], v[54:57], off offset:192
	s_waitcnt lgkmcnt(0)
	s_barrier
	s_branch .LBB1_6
